# speedup vs baseline: 1.0070x; 1.0070x over previous
.LBB0_4:
	s_or_b64 exec, exec, s[6:7]
	v_lshrrev_b32_e32 v87, 1, v1
	v_lshrrev_b32_e32 v88, 6, v0
	v_lshlrev_b32_e32 v88, 3, v88
	v_xor_b32_e32 v88, v88, v87
	v_lshlrev_b32_e32 v88, 4, v88
	v_lshl_or_b32 v87, v87, 9, v88
	v_and_b32_e32 v88, 1, v1
	v_lshl_or_b32 v87, v88, 3, v87
	v_lshrrev_b32_e32 v88, 5, v0
	v_and_b32_e32 v89, 31, v0
	v_xor_b32_e32 v89, v89, v88
	v_lshlrev_b32_e32 v89, 4, v89
	v_lshl_or_b32 v88, v88, 9, v89
	v_lshlrev_b32_e32 v89, 4, v0
	s_waitcnt vmcnt(14)
	v_mul_f32_e32 v67, v63, v63
	v_fmac_f32_e32 v67, v62, v62
	v_fmac_f32_e32 v67, v64, v64
	v_fmac_f32_e32 v67, v65, v65
	v_fmac_f32_e32 v67, v58, v58
	v_fmac_f32_e32 v67, v59, v59
	v_fmac_f32_e32 v67, v60, v60
	v_fmac_f32_e32 v67, v61, v61
	v_add_f32_e32 v75, v62, v63
	v_add_f32_e32 v83, v64, v65
	v_add_f32_e32 v75, v75, v83
	v_add_f32_e32 v84, v58, v59
	v_add_f32_e32 v85, v60, v61
	v_add_f32_e32 v84, v84, v85
	v_add_f32_e32 v75, v75, v84
	s_waitcnt vmcnt(12)
	v_mul_f32_e32 v68, v51, v51
	v_fmac_f32_e32 v68, v50, v50
	v_fmac_f32_e32 v68, v52, v52
	v_fmac_f32_e32 v68, v53, v53
	v_fmac_f32_e32 v68, v46, v46
	v_fmac_f32_e32 v68, v47, v47
	v_fmac_f32_e32 v68, v48, v48
	v_fmac_f32_e32 v68, v49, v49
	v_add_f32_e32 v76, v50, v51
	v_add_f32_e32 v83, v52, v53
	v_add_f32_e32 v76, v76, v83
	v_add_f32_e32 v84, v46, v47
	v_add_f32_e32 v85, v48, v49
	v_add_f32_e32 v84, v84, v85
	v_add_f32_e32 v76, v76, v84
	s_waitcnt vmcnt(8)
	v_mul_f32_e32 v71, v31, v31
	v_fmac_f32_e32 v71, v30, v30
	v_fmac_f32_e32 v71, v32, v32
	v_fmac_f32_e32 v71, v33, v33
	v_fmac_f32_e32 v71, v26, v26
	v_fmac_f32_e32 v71, v27, v27
	v_fmac_f32_e32 v71, v28, v28
	v_fmac_f32_e32 v71, v29, v29
	v_add_f32_e32 v79, v30, v31
	v_add_f32_e32 v83, v32, v33
	v_add_f32_e32 v79, v79, v83
	v_add_f32_e32 v84, v26, v27
	v_add_f32_e32 v85, v28, v29
	v_add_f32_e32 v84, v84, v85
	v_add_f32_e32 v79, v79, v84
	s_waitcnt vmcnt(6)
	v_mul_f32_e32 v72, v23, v23
	v_fmac_f32_e32 v72, v22, v22
	v_fmac_f32_e32 v72, v24, v24
	v_fmac_f32_e32 v72, v25, v25
	v_fmac_f32_e32 v72, v18, v18
	v_fmac_f32_e32 v72, v19, v19
	v_fmac_f32_e32 v72, v20, v20
	v_fmac_f32_e32 v72, v21, v21
	v_add_f32_e32 v80, v22, v23
	v_add_f32_e32 v83, v24, v25
	v_add_f32_e32 v80, v80, v83
	v_add_f32_e32 v84, v18, v19
	v_add_f32_e32 v85, v20, v21
	v_add_f32_e32 v84, v84, v85
	v_add_f32_e32 v80, v80, v84
	s_waitcnt vmcnt(5)
	v_mul_f32_e32 v70, v35, v35
	v_fmac_f32_e32 v70, v34, v34
	v_fmac_f32_e32 v70, v36, v36
	v_fmac_f32_e32 v70, v37, v37
	v_fmac_f32_e32 v70, v38, v38
	v_fmac_f32_e32 v70, v39, v39
	v_fmac_f32_e32 v70, v40, v40
	v_fmac_f32_e32 v70, v41, v41
	v_add_f32_e32 v78, v34, v35
	v_add_f32_e32 v83, v36, v37
	v_add_f32_e32 v78, v78, v83
	v_add_f32_e32 v84, v38, v39
	v_add_f32_e32 v85, v40, v41
	v_add_f32_e32 v84, v84, v85
	v_add_f32_e32 v78, v78, v84
	s_waitcnt vmcnt(3)
	v_mul_f32_e32 v73, v15, v15
	v_fmac_f32_e32 v73, v14, v14
	v_fmac_f32_e32 v73, v16, v16
	v_fmac_f32_e32 v73, v17, v17
	v_fmac_f32_e32 v73, v10, v10
	v_fmac_f32_e32 v73, v11, v11
	v_fmac_f32_e32 v73, v12, v12
	v_fmac_f32_e32 v73, v13, v13
	v_add_f32_e32 v81, v14, v15
	v_add_f32_e32 v83, v16, v17
	v_add_f32_e32 v81, v81, v83
	v_add_f32_e32 v84, v10, v11
	v_add_f32_e32 v85, v12, v13
	v_add_f32_e32 v84, v84, v85
	v_add_f32_e32 v81, v81, v84
	s_waitcnt vmcnt(1)
	v_mul_f32_e32 v69, v55, v55
	v_fmac_f32_e32 v69, v54, v54
	v_fmac_f32_e32 v69, v56, v56
	v_fmac_f32_e32 v69, v57, v57
	v_fmac_f32_e32 v69, v42, v42
	v_fmac_f32_e32 v69, v43, v43
	v_fmac_f32_e32 v69, v44, v44
	v_fmac_f32_e32 v69, v45, v45
	v_add_f32_e32 v77, v54, v55
	v_add_f32_e32 v83, v56, v57
	v_add_f32_e32 v77, v77, v83
	v_add_f32_e32 v84, v42, v43
	v_add_f32_e32 v85, v44, v45
	v_add_f32_e32 v84, v84, v85
	v_add_f32_e32 v77, v77, v84
	s_waitcnt vmcnt(0)
	v_mul_f32_e32 v74, v7, v7
	v_fmac_f32_e32 v74, v6, v6
	v_fmac_f32_e32 v74, v8, v8
	v_fmac_f32_e32 v74, v9, v9
	v_fmac_f32_e32 v74, v2, v2
	v_fmac_f32_e32 v74, v3, v3
	v_fmac_f32_e32 v74, v4, v4
	v_fmac_f32_e32 v74, v5, v5
	v_add_f32_e32 v82, v6, v7
	v_add_f32_e32 v83, v8, v9
	v_add_f32_e32 v82, v82, v83
	v_add_f32_e32 v84, v2, v3
	v_add_f32_e32 v85, v4, v5
	v_add_f32_e32 v84, v84, v85
	v_add_f32_e32 v82, v82, v84
	v_and_b32_e32 v83, 8, v0
	v_cmp_ne_u32_e64 s[6:7], 0, v83
	v_permlane32_swap_b32_e32 v67, v71
	v_permlane32_swap_b32_e32 v75, v79
	v_permlane32_swap_b32_e32 v68, v72
	v_permlane32_swap_b32_e32 v76, v80
	v_permlane32_swap_b32_e32 v69, v73
	v_permlane32_swap_b32_e32 v77, v81
	v_permlane32_swap_b32_e32 v70, v74
	v_permlane32_swap_b32_e32 v78, v82
	v_add_f32_e32 v67, v67, v71
	v_add_f32_e32 v75, v75, v79
	v_add_f32_e32 v68, v68, v72
	v_add_f32_e32 v76, v76, v80
	v_add_f32_e32 v69, v69, v73
	v_add_f32_e32 v77, v77, v81
	v_add_f32_e32 v70, v70, v74
	v_add_f32_e32 v78, v78, v82
	s_nop 1
	v_permlane16_swap_b32_e32 v67, v69
	v_permlane16_swap_b32_e32 v75, v77
	v_permlane16_swap_b32_e32 v68, v70
	v_permlane16_swap_b32_e32 v76, v78
	v_add_f32_e32 v67, v67, v69
	v_add_f32_e32 v75, v75, v77
	v_add_f32_e32 v68, v68, v70
	v_add_f32_e32 v76, v76, v78
	v_cndmask_b32_e64 v83, v67, v68, s[6:7]
	v_cndmask_b32_e64 v84, v68, v67, s[6:7]
	v_cndmask_b32_e64 v85, v75, v76, s[6:7]
	v_cndmask_b32_e64 v86, v76, v75, s[6:7]
	s_nop 1
	v_add_f32_dpp v67, v84, v83 row_ror:8 row_mask:0xf bank_mask:0xf
	v_add_f32_dpp v69, v86, v85 row_ror:8 row_mask:0xf bank_mask:0xf
	s_nop 1
	v_add_f32_dpp v67, v67, v67 row_half_mirror row_mask:0xf bank_mask:0xf
	v_add_f32_dpp v69, v69, v69 row_half_mirror row_mask:0xf bank_mask:0xf
	s_nop 1
	v_add_f32_dpp v67, v67, v67 quad_perm:[2,3,0,1] row_mask:0xf bank_mask:0xf
	v_add_f32_dpp v69, v69, v69 quad_perm:[2,3,0,1] row_mask:0xf bank_mask:0xf
	s_nop 1
	v_add_f32_dpp v67, v67, v67 quad_perm:[1,0,3,2] row_mask:0xf bank_mask:0xf
	v_add_f32_dpp v69, v69, v69 quad_perm:[1,0,3,2] row_mask:0xf bank_mask:0xf
	s_mov_b32 s3, 0xf800000
	v_mul_f32_e32 v70, 0x4f800000, v67
	v_cmp_gt_f32_e32 vcc, s3, v67
	s_nop 1
	v_cndmask_b32_e32 v67, v67, v70, vcc
	v_sqrt_f32_e32 v70, v67
	s_nop 0
	v_add_u32_e32 v68, -1, v70
	v_fma_f32 v73, -v68, v70, v67
	v_cmp_ge_f32_e64 s[4:5], 0, v73
	v_add_u32_e32 v73, 1, v70
	s_nop 0
	v_cndmask_b32_e64 v68, v70, v68, s[4:5]
	v_fma_f32 v70, -v73, v70, v67
	v_cmp_lt_f32_e64 s[4:5], 0, v70
	s_nop 1
	v_cndmask_b32_e64 v68, v68, v73, s[4:5]
	v_mul_f32_e32 v70, 0x37800000, v68
	v_cndmask_b32_e32 v68, v68, v70, vcc
	v_mov_b32_e32 v70, 0x260
	v_cmp_class_f32_e32 vcc, v67, v70
	s_nop 1
	v_cndmask_b32_e32 v67, v68, v67, vcc
	v_max_f32_e32 v68, 0x322bcc77, v67
	v_div_scale_f32 v67, s[4:5], v68, v68, 1.0
	v_rcp_f32_e32 v73, v67
	s_load_dwordx2 s[4:5], s[0:1], 0x8
	v_fma_f32 v71, -v67, v73, 1.0
	v_fmac_f32_e32 v73, v71, v73
	v_div_scale_f32 v71, vcc, 1.0, v68, 1.0
	v_mul_f32_e32 v72, v71, v73
	v_fma_f32 v74, -v67, v72, v71
	v_fmac_f32_e32 v72, v74, v73
	v_fma_f32 v67, -v67, v72, v71
	v_div_fmas_f32 v71, v67, v73, v72
	v_mov_b32_e32 v70, 0
	v_and_b32_e32 v67, 7, v0
	v_cmp_ne_u32_e32 vcc, 0, v67
	v_lshlrev_b32_e32 v67, 3, v66
	s_and_saveexec_b64 s[6:7], vcc
	s_xor_b64 s[6:7], exec, s[6:7]
	v_lshlrev_b32_e32 v67, 3, v66
	s_or_saveexec_b64 s[6:7], s[6:7]
	v_div_fixup_f32 v66, v71, v68, 1.0
	s_xor_b64 exec, exec, s[6:7]
	s_cbranch_execz .LBB0_10
	s_load_dwordx2 s[0:1], s[0:1], 0x10
	s_waitcnt lgkmcnt(0)
	v_add_f32_e32 v68, v69, v70
	v_mul_f32_e32 v70, v68, v66
	s_lshl_b32 s3, s2, 5
	v_lshrrev_b32_e32 v68, 3, v1
	v_or3_b32 v68, v67, s3, v68
	v_ashrrev_i32_e32 v69, 31, v68
	v_lshl_add_u64 v[68:69], v[68:69], 2, s[0:1]
	global_store_dword v[68:69], v70, off
.LBB0_10:
	s_or_b64 exec, exec, s[6:7]
	v_readlane_b32 s12, v66, 0
	v_readlane_b32 s14, v66, 8
	v_readlane_b32 s16, v66, 16
	v_readlane_b32 s18, v66, 24
	v_readlane_b32 s20, v66, 32
	v_readlane_b32 s22, v66, 40
	v_readlane_b32 s24, v66, 48
	v_readlane_b32 s26, v66, 56
	s_nop 1
	v_pk_mul_f32 v[62:63], v[62:63], s[12:13] op_sel_hi:[1,0]
	v_pk_mul_f32 v[64:65], v[64:65], s[12:13] op_sel_hi:[1,0]
	v_pk_mul_f32 v[58:59], v[58:59], s[12:13] op_sel_hi:[1,0]
	v_pk_mul_f32 v[60:61], v[60:61], s[12:13] op_sel_hi:[1,0]
	v_cvt_pk_bf16_f32 v62, v62, v63
	v_cvt_pk_bf16_f32 v63, v64, v65
	v_cvt_pk_bf16_f32 v58, v58, v59
	v_cvt_pk_bf16_f32 v59, v60, v61
	ds_write_b64 v87, v[62:63]
	ds_write_b64 v87, v[58:59] offset:16384
	v_pk_mul_f32 v[50:51], v[50:51], s[14:15] op_sel_hi:[1,0]
	v_pk_mul_f32 v[52:53], v[52:53], s[14:15] op_sel_hi:[1,0]
	v_pk_mul_f32 v[46:47], v[46:47], s[14:15] op_sel_hi:[1,0]
	v_pk_mul_f32 v[48:49], v[48:49], s[14:15] op_sel_hi:[1,0]
	v_cvt_pk_bf16_f32 v50, v50, v51
	v_cvt_pk_bf16_f32 v51, v52, v53
	v_cvt_pk_bf16_f32 v46, v46, v47
	v_cvt_pk_bf16_f32 v47, v48, v49
	v_xor_b32_e32 v68, 16, v87
	ds_write_b64 v68, v[50:51]
	ds_write_b64 v68, v[46:47] offset:16384
	v_pk_mul_f32 v[54:55], v[54:55], s[16:17] op_sel_hi:[1,0]
	v_pk_mul_f32 v[56:57], v[56:57], s[16:17] op_sel_hi:[1,0]
	v_pk_mul_f32 v[42:43], v[42:43], s[16:17] op_sel_hi:[1,0]
	v_pk_mul_f32 v[44:45], v[44:45], s[16:17] op_sel_hi:[1,0]
	v_cvt_pk_bf16_f32 v54, v54, v55
	v_cvt_pk_bf16_f32 v55, v56, v57
	v_cvt_pk_bf16_f32 v42, v42, v43
	v_cvt_pk_bf16_f32 v43, v44, v45
	v_xor_b32_e32 v69, 32, v87
	ds_write_b64 v69, v[54:55]
	ds_write_b64 v69, v[42:43] offset:16384
	v_pk_mul_f32 v[34:35], v[34:35], s[18:19] op_sel_hi:[1,0]
	v_pk_mul_f32 v[36:37], v[36:37], s[18:19] op_sel_hi:[1,0]
	v_pk_mul_f32 v[38:39], v[38:39], s[18:19] op_sel_hi:[1,0]
	v_pk_mul_f32 v[40:41], v[40:41], s[18:19] op_sel_hi:[1,0]
	v_cvt_pk_bf16_f32 v34, v34, v35
	v_cvt_pk_bf16_f32 v35, v36, v37
	v_cvt_pk_bf16_f32 v38, v38, v39
	v_cvt_pk_bf16_f32 v39, v40, v41
	v_xor_b32_e32 v70, 48, v87
	ds_write_b64 v70, v[34:35]
	ds_write_b64 v70, v[38:39] offset:16384
	v_pk_mul_f32 v[30:31], v[30:31], s[20:21] op_sel_hi:[1,0]
	v_pk_mul_f32 v[32:33], v[32:33], s[20:21] op_sel_hi:[1,0]
	v_pk_mul_f32 v[26:27], v[26:27], s[20:21] op_sel_hi:[1,0]
	v_pk_mul_f32 v[28:29], v[28:29], s[20:21] op_sel_hi:[1,0]
	v_cvt_pk_bf16_f32 v30, v30, v31
	v_cvt_pk_bf16_f32 v31, v32, v33
	v_cvt_pk_bf16_f32 v26, v26, v27
	v_cvt_pk_bf16_f32 v27, v28, v29
	v_xor_b32_e32 v71, 64, v87
	ds_write_b64 v71, v[30:31]
	ds_write_b64 v71, v[26:27] offset:16384
	v_pk_mul_f32 v[22:23], v[22:23], s[22:23] op_sel_hi:[1,0]
	v_pk_mul_f32 v[24:25], v[24:25], s[22:23] op_sel_hi:[1,0]
	v_pk_mul_f32 v[18:19], v[18:19], s[22:23] op_sel_hi:[1,0]
	v_pk_mul_f32 v[20:21], v[20:21], s[22:23] op_sel_hi:[1,0]
	v_cvt_pk_bf16_f32 v22, v22, v23
	v_cvt_pk_bf16_f32 v23, v24, v25
	v_cvt_pk_bf16_f32 v18, v18, v19
	v_cvt_pk_bf16_f32 v19, v20, v21
	v_xor_b32_e32 v72, 80, v87
	ds_write_b64 v72, v[22:23]
	ds_write_b64 v72, v[18:19] offset:16384
	v_pk_mul_f32 v[14:15], v[14:15], s[24:25] op_sel_hi:[1,0]
	v_pk_mul_f32 v[16:17], v[16:17], s[24:25] op_sel_hi:[1,0]
	v_pk_mul_f32 v[10:11], v[10:11], s[24:25] op_sel_hi:[1,0]
	v_pk_mul_f32 v[12:13], v[12:13], s[24:25] op_sel_hi:[1,0]
	v_cvt_pk_bf16_f32 v14, v14, v15
	v_cvt_pk_bf16_f32 v15, v16, v17
	v_cvt_pk_bf16_f32 v10, v10, v11
	v_cvt_pk_bf16_f32 v11, v12, v13
	v_xor_b32_e32 v73, 96, v87
	ds_write_b64 v73, v[14:15]
	ds_write_b64 v73, v[10:11] offset:16384
	v_pk_mul_f32 v[6:7], v[6:7], s[26:27] op_sel_hi:[1,0]
	v_pk_mul_f32 v[8:9], v[8:9], s[26:27] op_sel_hi:[1,0]
	v_pk_mul_f32 v[2:3], v[2:3], s[26:27] op_sel_hi:[1,0]
	v_pk_mul_f32 v[4:5], v[4:5], s[26:27] op_sel_hi:[1,0]
	v_cvt_pk_bf16_f32 v6, v6, v7
	v_cvt_pk_bf16_f32 v7, v8, v9
	v_cvt_pk_bf16_f32 v2, v2, v3
	v_cvt_pk_bf16_f32 v3, v4, v5
	v_xor_b32_e32 v74, 112, v87
	ds_write_b64 v74, v[6:7]
	ds_write_b64 v74, v[2:3] offset:16384
	v_xor_b32_e32 v68, 0x80, v88
	v_xor_b32_e32 v69, 0x100, v88
	v_xor_b32_e32 v70, 0x180, v88
	s_lshl_b32 s8, s2, 15
	s_waitcnt lgkmcnt(0)
	s_and_b32 s5, s5, 0xffff
	s_mov_b32 s7, 0x20000
	s_brev_b32 s6, 64
	s_barrier
	ds_read_b128 v[2:5], v88
	ds_read_b128 v[6:9], v68 offset:4096
	ds_read_b128 v[10:13], v69 offset:8192
	ds_read_b128 v[14:17], v70 offset:12288
	ds_read_b128 v[18:21], v88 offset:16384
	ds_read_b128 v[22:25], v68 offset:20480
	ds_read_b128 v[26:29], v69 offset:24576
	ds_read_b128 v[30:33], v70 offset:28672
	s_waitcnt lgkmcnt(7)
	buffer_store_dwordx4 v[2:5], v89, s[4:7], s8 offen sc1
	s_add_u32 s8, s8, 0x1000
	s_waitcnt lgkmcnt(6)
	buffer_store_dwordx4 v[6:9], v89, s[4:7], s8 offen sc1
	s_add_u32 s8, s8, 0x1000
	s_waitcnt lgkmcnt(5)
	buffer_store_dwordx4 v[10:13], v89, s[4:7], s8 offen sc1
	s_add_u32 s8, s8, 0x1000
	s_waitcnt lgkmcnt(4)
	buffer_store_dwordx4 v[14:17], v89, s[4:7], s8 offen sc1
	s_add_u32 s8, s8, 0x1000
	s_waitcnt lgkmcnt(3)
	buffer_store_dwordx4 v[18:21], v89, s[4:7], s8 offen sc1
	s_add_u32 s8, s8, 0x1000
	s_waitcnt lgkmcnt(2)
	buffer_store_dwordx4 v[22:25], v89, s[4:7], s8 offen sc1
	s_add_u32 s8, s8, 0x1000
	s_waitcnt lgkmcnt(1)
	buffer_store_dwordx4 v[26:29], v89, s[4:7], s8 offen sc1
	s_add_u32 s8, s8, 0x1000
	s_waitcnt lgkmcnt(0)
	buffer_store_dwordx4 v[30:33], v89, s[4:7], s8 offen sc1
	s_endpgm

	.amdhsa_kernel _Z6k_normPKfP15HIP_vector_typeIjLj4EEPfPyS4_
		.amdhsa_group_segment_fixed_size 32768
		.amdhsa_private_segment_fixed_size 0
		.amdhsa_kernarg_size 40
		.amdhsa_user_sgpr_count 2
		.amdhsa_user_sgpr_dispatch_ptr 0
		.amdhsa_user_sgpr_queue_ptr 0
		.amdhsa_user_sgpr_kernarg_segment_ptr 1
		.amdhsa_user_sgpr_dispatch_id 0
		.amdhsa_user_sgpr_kernarg_preload_length 0
		.amdhsa_user_sgpr_kernarg_preload_offset 0
		.amdhsa_user_sgpr_private_segment_size 0
		.amdhsa_uses_dynamic_stack 0
		.amdhsa_enable_private_segment 0
		.amdhsa_system_sgpr_workgroup_id_x 1
		.amdhsa_system_sgpr_workgroup_id_y 0
		.amdhsa_system_sgpr_workgroup_id_z 0
		.amdhsa_system_sgpr_workgroup_info 0
		.amdhsa_system_vgpr_workitem_id 0
		.amdhsa_next_free_vgpr 90
		.amdhsa_next_free_sgpr 96
		.amdhsa_accum_offset 92
		.amdhsa_reserve_vcc 1
		.amdhsa_float_round_mode_32 0
		.amdhsa_float_round_mode_16_64 0
		.amdhsa_float_denorm_mode_32 3
		.amdhsa_float_denorm_mode_16_64 3
		.amdhsa_dx10_clamp 1
		.amdhsa_ieee_mode 1
		.amdhsa_fp16_overflow 0
		.amdhsa_tg_split 0
		.amdhsa_exception_fp_ieee_invalid_op 0
		.amdhsa_exception_fp_denorm_src 0
		.amdhsa_exception_fp_ieee_div_zero 0
		.amdhsa_exception_fp_ieee_overflow 0
		.amdhsa_exception_fp_ieee_underflow 0
		.amdhsa_exception_fp_ieee_inexact 0
		.amdhsa_exception_int_div_zero 0
	.end_amdhsa_kernel

amdhsa.kernels:
  - .agpr_count:     0
    .args:
      - .actual_access:  read_only
        .address_space:  global
        .offset:         0
        .size:           8
        .value_kind:     global_buffer
      - .actual_access:  write_only
        .address_space:  global
        .offset:         8
        .size:           8
        .value_kind:     global_buffer
      - .actual_access:  write_only
        .address_space:  global
        .offset:         16
        .size:           8
        .value_kind:     global_buffer
      - .actual_access:  write_only
        .address_space:  global
        .offset:         24
        .size:           8
        .value_kind:     global_buffer
      - .actual_access:  write_only
        .address_space:  global
        .offset:         32
        .size:           8
        .value_kind:     global_buffer
    .group_segment_fixed_size: 32768
    .kernarg_segment_align: 8
    .kernarg_segment_size: 40
    .language:       OpenCL C
    .language_version:
      - 2
      - 0
    .max_flat_workgroup_size: 256
    .name:           _Z6k_normPKfP15HIP_vector_typeIjLj4EEPfPyS4_
    .private_segment_fixed_size: 0
    .sgpr_count:     16
    .sgpr_spill_count: 0
    .symbol:         _Z6k_normPKfP15HIP_vector_typeIjLj4EEPfPyS4_.kd
    .uniform_work_group_size: 1
    .uses_dynamic_stack: false
    .vgpr_count:     90
    .vgpr_spill_count: 0
    .wavefront_size: 64
  - .agpr_count:     0
    .args:
      - .actual_access:  read_only
        .address_space:  global
        .offset:         0
        .size:           8
        .value_kind:     global_buffer
      - .actual_access:  read_only
        .address_space:  global
        .offset:         8
        .size:           8
        .value_kind:     global_buffer
      - .actual_access:  read_only
        .address_space:  global
        .offset:         16
        .size:           8
        .value_kind:     global_buffer
      - .actual_access:  read_only
        .address_space:  global
        .offset:         24
        .size:           8
        .value_kind:     global_buffer
      - .address_space:  global
        .offset:         32
        .size:           8
        .value_kind:     global_buffer
    .group_segment_fixed_size: 64
    .kernarg_segment_align: 8
    .kernarg_segment_size: 40
    .language:       OpenCL C
    .language_version:
      - 2
      - 0
    .max_flat_workgroup_size: 1024
    .name:           _Z6k_distPKyPKfS2_PK15HIP_vector_typeIjLj4EEPf
    .private_segment_fixed_size: 0
    .sgpr_count:     16
    .sgpr_spill_count: 0
    .symbol:         _Z6k_distPKyPKfS2_PK15HIP_vector_typeIjLj4EEPf.kd
    .uniform_work_group_size: 1
    .uses_dynamic_stack: false
    .vgpr_count:     17
    .vgpr_spill_count: 0
    .wavefront_size: 64
  - .agpr_count:     0
    .args:
      - .actual_access:  read_only
        .address_space:  global
        .offset:         0
        .size:           8
        .value_kind:     global_buffer
      - .actual_access:  write_only
        .address_space:  global
        .offset:         8
        .size:           8
        .value_kind:     global_buffer
    .group_segment_fixed_size: 0
    .kernarg_segment_align: 8
    .kernarg_segment_size: 16
    .language:       OpenCL C
    .language_version:
      - 2
      - 0
    .max_flat_workgroup_size: 64
    .name:           _Z7k_finalPKfPf
    .private_segment_fixed_size: 0
    .sgpr_count:     12
    .sgpr_spill_count: 0
    .symbol:         _Z7k_finalPKfPf.kd
    .uniform_work_group_size: 1
    .uses_dynamic_stack: false
    .vgpr_count:     6
    .vgpr_spill_count: 0
    .wavefront_size: 64
  - .agpr_count:     0
    .args:
      - .address_space:  global
        .offset:         0
        .size:           8
        .value_kind:     global_buffer
      - .address_space:  global
        .offset:         8
        .size:           8
        .value_kind:     global_buffer
      - .actual_access:  write_only
        .address_space:  global
        .offset:         16
        .size:           8
        .value_kind:     global_buffer
    .group_segment_fixed_size: 133120
    .kernarg_segment_align: 8
    .kernarg_segment_size: 24
    .language:       OpenCL C
    .language_version:
      - 2
      - 0
    .max_flat_workgroup_size: 512
    .name:           _Z6k_gramILi0EEvPK15HIP_vector_typeIjLj4EEPyPf
    .private_segment_fixed_size: 0
    .sgpr_count:     64
    .sgpr_spill_count: 0
    .symbol:         _Z6k_gramILi0EEvPK15HIP_vector_typeIjLj4EEPyPf.kd
    .uniform_work_group_size: 1
    .uses_dynamic_stack: false
    .vgpr_count:     240
    .vgpr_spill_count: 0
    .wavefront_size: 64
